# speedup vs baseline: 1.0006x; 1.0006x over previous
.LBB2_12:
	s_add_i32 s16, s22, 0xffffc000
	s_and_b32 s16, s16, 0xc000
	v_add_u32_e32 v116, s16, v108
	s_add_u32 s16, s12, 0xfffce000
	s_addc_u32 s17, s13, -1
	v_readfirstlane_b32 s26, v116
	v_lshl_add_u64 v[116:117], s[16:17], 0, v[84:85]
	s_mov_b32 m0, s26
	s_nop 0
	global_load_lds_dwordx4 v[116:117], off
	v_lshl_add_u64 v[116:117], s[16:17], 0, v[86:87]
	s_add_i32 s16, s26, 0x400
	s_mov_b32 m0, s16
	s_nop 0
	global_load_lds_dwordx4 v[116:117], off
	s_and_b32 s16, s22, 0xc000
	v_add_u32_e32 v116, s16, v108
	s_nop 0
	v_readfirstlane_b32 s16, v116
	v_lshl_add_u64 v[116:117], s[12:13], 0, v[84:85]
	s_mov_b32 m0, s16
	s_nop 0
	global_load_lds_dwordx4 v[116:117], off
	v_lshl_add_u64 v[116:117], s[12:13], 0, v[86:87]
	s_addk_i32 s16, 0x400
	s_mov_b32 m0, s16
	s_nop 0
	global_load_lds_dwordx4 v[116:117], off
	v_cmp_neq_f32_e32 vcc, s25, v102
	v_add_u32_e32 v114, v114, v98
	v_add_u32_e32 v107, 2, v107
	v_cndmask_b32_e64 v124, v112, -v102, vcc
	v_fmamk_f32 v34, v34, 0x3e38aa3b, v124
	v_fmamk_f32 v50, v50, 0x3e38aa3b, v124
	v_exp_f32_e32 v126, v34
	v_fmamk_f32 v34, v51, 0x3e38aa3b, v124
	v_exp_f32_e32 v125, v50
	v_exp_f32_e32 v82, v34
	v_fmamk_f32 v34, v35, 0x3e38aa3b, v124
	v_exp_f32_e32 v34, v34
	v_add_f32_e32 v35, v126, v125
	v_fmamk_f32 v36, v36, 0x3e38aa3b, v124
	v_exp_f32_e32 v127, v36
	v_add_f32_e32 v50, v34, v82
	v_add_f32_e32 v51, v35, v83
	v_fmamk_f32 v35, v52, 0x3e38aa3b, v124
	v_add_f32_e32 v89, v50, v51
	v_fmamk_f32 v36, v53, 0x3e38aa3b, v124
	v_exp_f32_e32 v35, v35
	v_exp_f32_e32 v88, v36
	v_fmamk_f32 v36, v37, 0x3e38aa3b, v124
	v_exp_f32_e32 v36, v36
	v_add_f32_e32 v37, v127, v35
	v_fmamk_f32 v38, v38, 0x3e38aa3b, v124
	v_exp_f32_e32 v115, v38
	v_add_f32_e32 v50, v36, v88
	v_add_f32_e32 v51, v37, v89
	v_fmamk_f32 v37, v54, 0x3e38aa3b, v124
	v_add_f32_e32 v91, v50, v51
	v_fmamk_f32 v38, v55, 0x3e38aa3b, v124
	v_exp_f32_e32 v37, v37
	v_exp_f32_e32 v90, v38
	v_fmamk_f32 v38, v39, 0x3e38aa3b, v124
	v_exp_f32_e32 v50, v38
	v_add_f32_e32 v51, v115, v37
	s_add_u32 s12, s12, 0x64000
	s_addc_u32 s13, s13, 0
	v_add_f32_e32 v38, v50, v90
	v_add_f32_e32 v39, v51, v91
	s_add_i32 s22, s22, 0x8000
	v_add_f32_e32 v55, v38, v39
	v_fmamk_f32 v38, v56, 0x3e38aa3b, v124
	v_exp_f32_e32 v51, v38
	v_fmamk_f32 v38, v40, 0x3e38aa3b, v124
	v_exp_f32_e32 v91, v38
	v_fmamk_f32 v38, v57, 0x3e38aa3b, v124
	v_exp_f32_e32 v54, v38
	v_fmamk_f32 v38, v41, 0x3e38aa3b, v124
	v_exp_f32_e32 v52, v38
	v_add_f32_e32 v53, v91, v51
	v_cvt_pk_f16_f32 v57, v51, v54
	v_cvt_pk_f16_f32 v56, v37, v90
	v_add_f32_e32 v38, v52, v54
	v_add_f32_e32 v39, v53, v55
	v_cvt_pk_f16_f32 v55, v35, v88
	v_add_f32_e32 v117, v38, v39
	v_fmamk_f32 v38, v58, 0x3e38aa3b, v124
	v_exp_f32_e32 v53, v38
	v_fmamk_f32 v38, v42, 0x3e38aa3b, v124
	v_exp_f32_e32 v1, v38
	v_fmamk_f32 v38, v59, 0x3e38aa3b, v124
	v_exp_f32_e32 v116, v38
	v_fmamk_f32 v38, v43, 0x3e38aa3b, v124
	v_exp_f32_e32 v38, v38
	v_add_f32_e32 v39, v1, v53
	v_cvt_pk_f16_f32 v54, v125, v82
	v_fmamk_f32 v35, v64, 0x3e38aa3b, v124
	v_add_f32_e32 v40, v38, v116
	v_add_f32_e32 v41, v39, v117
	v_fmamk_f32 v39, v60, 0x3e38aa3b, v124
	v_add_f32_e32 v119, v40, v41
	v_fmamk_f32 v40, v44, 0x3e38aa3b, v124
	v_exp_f32_e32 v117, v40
	v_fmamk_f32 v40, v61, 0x3e38aa3b, v124
	v_exp_f32_e32 v39, v39
	v_exp_f32_e32 v118, v40
	v_fmamk_f32 v40, v45, 0x3e38aa3b, v124
	v_exp_f32_e32 v40, v40
	v_add_f32_e32 v41, v117, v39
	v_exp_f32_e32 v82, v35
	v_fmamk_f32 v35, v65, 0x3e38aa3b, v124
	v_add_f32_e32 v42, v40, v118
	v_add_f32_e32 v43, v41, v119
	v_fmamk_f32 v41, v62, 0x3e38aa3b, v124
	v_add_f32_e32 v121, v42, v43
	v_fmamk_f32 v42, v46, 0x3e38aa3b, v124
	v_exp_f32_e32 v119, v42
	v_fmamk_f32 v42, v63, 0x3e38aa3b, v124
	v_exp_f32_e32 v41, v41
	v_exp_f32_e32 v120, v42
	v_fmamk_f32 v42, v47, 0x3e38aa3b, v124
	v_exp_f32_e32 v122, v42
	ds_read_b64_tr_b16 v[42:43], v114 offset:8192
	ds_read_b64_tr_b16 v[44:45], v114 offset:8704
	v_add_f32_e32 v123, v119, v41
	ds_read_b64_tr_b16 v[58:59], v114 offset:9216
	ds_read_b64_tr_b16 v[60:61], v114 offset:9728
	v_add_f32_e32 v46, v122, v120
	v_add_f32_e32 v47, v123, v121
	s_waitcnt lgkmcnt(2)
	v_mfma_f32_32x32x16_f16 v[18:33], v[54:57], v[42:45], v[18:33]
	v_add_f32_e64 v88, v46, v46
	v_add_f32_e64 v89, v46, v47
	ds_read_b64_tr_b16 v[42:43], v114 offset:12288
	ds_read_b64_tr_b16 v[44:45], v114 offset:12800
	v_exp_f32_e32 v88, v35
	ds_read_b64_tr_b16 v[62:63], v114 offset:13312
	ds_read_b64_tr_b16 v[64:65], v114 offset:13824
	v_cvt_pk_f16_f32 v51, v127, v36
	v_cmp_le_u32_e32 vcc, s21, v107
	s_or_b64 s[14:15], vcc, s[14:15]
	s_waitcnt lgkmcnt(2)
	v_mfma_f32_32x32x16_f16 v[2:17], v[54:57], v[42:45], v[2:17]
	v_cvt_pk_f16_f32 v45, v82, v88
	v_cvt_pk_f16_f32 v44, v41, v120
	v_cvt_pk_f16_f32 v43, v39, v118
	v_cvt_pk_f16_f32 v42, v53, v116
	v_cvt_pk_f16_f32 v53, v91, v52
	v_cvt_pk_f16_f32 v52, v115, v50
	v_cvt_pk_f16_f32 v50, v126, v34
	v_mfma_f32_32x32x16_f16 v[18:33], v[42:45], v[58:61], v[18:33]
	v_fmamk_f32 v39, v48, 0x3e38aa3b, v124
	v_fmac_f32_e32 v124, 0x3e38aa3b, v49
	v_exp_f32_e32 v39, v39
	v_exp_f32_e32 v54, v124
	v_cvt_pk_f16_f32 v41, v117, v40
	v_cvt_pk_f16_f32 v40, v1, v38
	v_add_f32_e32 v55, v39, v82
	s_waitcnt lgkmcnt(0)
	v_mfma_f32_32x32x16_f16 v[2:17], v[42:45], v[62:65], v[2:17]
	ds_read_b64_tr_b16 v[42:43], v114 offset:10240
	ds_read_b64_tr_b16 v[44:45], v114 offset:10752
	ds_read_b64_tr_b16 v[34:35], v114 offset:11264
	ds_read_b64_tr_b16 v[36:37], v114 offset:11776
	s_waitcnt lgkmcnt(2)
	v_mfma_f32_32x32x16_f16 v[18:33], v[50:53], v[42:45], v[18:33]
	ds_read_b64_tr_b16 v[42:43], v114 offset:14336
	ds_read_b64_tr_b16 v[44:45], v114 offset:14848
	ds_read_b64_tr_b16 v[46:47], v114 offset:15360
	ds_read_b64_tr_b16 v[48:49], v114 offset:15872
	s_waitcnt lgkmcnt(2)
	v_mfma_f32_32x32x16_f16 v[2:17], v[50:53], v[42:45], v[2:17]
	v_cvt_pk_f16_f32 v43, v39, v54
	v_cvt_pk_f16_f32 v42, v119, v122
	s_nop 1
	v_mfma_f32_32x32x16_f16 v[18:33], v[40:43], v[34:37], v[18:33]
	v_add_f32_e64 v34, v54, v88
	v_add_f32_e64 v35, v55, v89
	v_mov_b32_e32 v88, v102
	v_add_f32_e32 v1, v34, v35
	v_add_f32_e32 v113, v113, v1
	s_waitcnt lgkmcnt(0)
	v_mfma_f32_32x32x16_f16 v[2:17], v[40:43], v[46:49], v[2:17]
	s_andn2_b64 exec, exec, s[14:15]
	s_cbranch_execz .LBB2_17
